# P9 SwiGLU epilogue: bias preloaded into the accumulators (64*b), scale folded into clamp bounds and sigmoid denominator, next-unit bias prefetched at epilogue start (replaces opt8)
# speedup vs baseline: 1.0088x; 1.0076x over previous
; #define LAS __attribute__((address_space(3)))
;     __device__ __forceinline__ void operator()(const f32x4 (&acc)[2][2][4][2], const Unit& u, int wr, int wc, int fr, int fq) const {
;     ...
;         f32x4 bv[2][2];
; #pragma unroll
;         for (int bj = 0; bj < 2; ++bj)
; #pragma unroll
;             for (int n = 0; n < 2; ++n) bv[bj][n] = *(const f32x4*)(bias + (size_t)e * bias_ld + col0 + bj * HALF + 4 * n);
;         LAS unsigned char* wp = stg + (16 * wr + fr) * STG8_PITCH + 16 * wc + 4 * fq;
;         const int rr = (tid >> 3) & 31, cc = tid & 7, ms = tid >> 8;
;         const LAS unsigned char* rp = stg + rr * STG8_PITCH + cc * 16;
;         unsigned char* gp = O + (size_t)(u.pm * BM + 64 * (rr >> 4) + (rr & 15)) * ldc + pnl * (BM / 2) + cc * 16;
.LBB0_991:
	s_min_i32 s40, s64, 64
	s_add_u32 s8, s96, 0xa1400000
	s_addc_u32 s9, s97, 0
	s_add_i32 s41, s31, 0x18000
	s_mov_b64 s[10:11], 0x80
	s_add_i32 s43, s31, 0x1a000
	v_lshl_add_u64 v[2:3], v[2:3], 0, s[10:11]
	s_mov_b32 m0, s41
	s_add_u32 s2, s24, 0x40080
	s_waitcnt vmcnt(2)
	s_barrier
	global_load_lds_dwordx4 v[2:3], off
	v_lshl_add_u64 v[2:3], v[4:5], 0, s[10:11]
	s_mov_b32 m0, s43
	s_addc_u32 s3, s25, 0
	s_add_i32 s44, s31, 0x1c000
	global_load_lds_dwordx4 v[2:3], off
	v_lshl_add_u64 v[2:3], s[2:3], 0, v[164:165]
	s_mov_b32 m0, s44
	s_add_i32 s45, s31, 0x1e000
	global_load_lds_dwordx4 v[2:3], off
	v_lshl_add_u64 v[2:3], s[2:3], 0, v[166:167]
	s_mov_b32 m0, s45
	s_cmpk_lt_u32 s12, 0x100
	global_load_lds_dwordx4 v[2:3], off
	v_lshlrev_b32_e32 v2, 3, v20
	v_lshl_or_b32 v200, s14, 5, v2
	v_lshl_or_b32 v2, s15, 4, v21
	s_movk_i32 s2, 0x90
	s_cselect_b64 s[12:13], -1, 0
	v_mul_lo_u32 v2, v2, s2
	s_lshl_b32 s2, s14, 4
	v_bfe_u32 v4, v0, 3, 5
	v_lshlrev_b32_e32 v6, 2, v22
	s_add_i32 s3, 0, 0x21000
	s_max_i32 s46, s40, 1
	s_waitcnt vmcnt(4)
	v_lshrrev_b32_e32 v5, 8, v0
	v_mul_u32_u24_e32 v4, 0x90, v4
	v_and_b32_e32 v170, 0x70, v18
	v_and_b32_e32 v6, 64, v6
	s_add_i32 s2, s2, s3
	s_add_i32 s46, s46, -1
	v_lshlrev_b32_e32 v3, 2, v20
	v_and_or_b32 v201, v22, 15, v6
	v_mul_u32_u24_e32 v6, 0x1200, v5
	v_lshlrev_b32_e32 v172, 15, v5
	v_add_u32_e32 v2, s2, v2
	v_add3_u32 v4, s3, v4, v170
	s_add_u32 s14, s96, 0x8ac00080
	v_mov_b32_e32 v171, v169
	v_or_b32_e32 v174, 0x10000, v172
	v_mov_b32_e32 v173, v169
	v_mov_b32_e32 v175, v169
	v_mov_b32_e32 v163, v169
	s_addc_u32 s15, s97, 0
	s_mov_b32 s16, 0x3c800000
	s_mov_b32 s47, 0xc3c00000
	v_add_u32_e32 v202, v2, v3
	v_add_u32_e32 v203, v4, v6
	s_mov_b32 s48, 0x40000
	v_mov_b32_e32 v204, 0x44000000
	v_mov_b32_e32 v246, 0x45800000
	v_mov_b32_e32 v247, 0x42800000
	s_ashr_i32 s2, s23, 31
	s_lshr_b32 s2, s2, 28
	s_add_i32 s3, s23, s2
	s_ashr_i32 s2, s3, 4
	s_and_b32 s3, s3, -16
	s_sub_i32 s54, s23, s3
	s_ashr_i32 s3, s2, 31
	s_lshl_b64 s[2:3], s[2:3], 14
	v_readlane_b32 s52, v254, 0
	v_lshl_or_b32 v2, s54, 8, v200
	v_readlane_b32 s53, v254, 1
	s_add_u32 s2, s52, s2
	s_addc_u32 s3, s53, s3
	v_ashrrev_i32_e32 v3, 31, v2
	v_lshl_add_u64 v[2:3], v[2:3], 2, s[2:3]
	global_load_dwordx4 v[208:211], v[2:3], off
	global_load_dwordx4 v[212:215], v[2:3], off offset:16
	global_load_dwordx4 v[216:219], v[2:3], off offset:512
	global_load_dwordx4 v[220:223], v[2:3], off offset:528
	s_waitcnt vmcnt(0)
	v_mul_f32_e32 v208, v247, v208
	v_fma_f32 v209, v209, v247, v247
	v_mul_f32_e32 v210, v247, v210
	v_fma_f32 v211, v211, v247, v247
	v_mul_f32_e32 v212, v247, v212
	v_fma_f32 v213, v213, v247, v247
	v_mul_f32_e32 v214, v247, v214
	v_fma_f32 v215, v215, v247, v247
	v_mul_f32_e32 v216, v247, v216
	v_fma_f32 v217, v217, v247, v247
	v_mul_f32_e32 v218, v247, v218
	v_fma_f32 v219, v219, v247, v247
	v_mul_f32_e32 v220, v247, v220
	v_fma_f32 v221, v221, v247, v247
	v_mul_f32_e32 v222, v247, v222
	v_fma_f32 v223, v223, v247, v247
	s_barrier
	s_branch .LBB0_994

.LBB0_1006:
	s_ashr_i32 s3, s19, 31
	s_mov_b32 s2, s19
	s_lshl_b64 s[2:3], s[2:3], 19
	s_add_u32 s20, s17, s2
	s_addc_u32 s21, s30, s3
	s_and_b64 s[2:3], s[26:27], exec
	s_cselect_b32 s2, s21, s25
	s_cselect_b32 s3, s20, s24
	v_mov_b32_e32 v181, v169
	v_mov_b32_e32 v179, v169
	v_mov_b32_e32 v177, v169
	v_mov_b32_e32 v183, v169
	s_add_u32 s50, s24, 0x100
	v_mov_b32_e32 v66, v220
	s_addc_u32 s51, s25, 0
	v_lshl_add_u64 v[184:185], s[14:15], 0, v[182:183]
	v_lshl_add_u64 v[186:187], s[14:15], 0, v[176:177]
	v_lshl_add_u64 v[188:189], s[14:15], 0, v[178:179]
	v_lshl_add_u64 v[190:191], s[14:15], 0, v[180:181]
	s_mov_b32 s52, -2
	s_mov_b64 s[28:29], 0
	v_mov_b32_e32 v67, v221
	v_mov_b32_e32 v68, v222
	v_mov_b32_e32 v69, v223
	v_mov_b32_e32 v70, v216
	v_mov_b32_e32 v71, v217
	v_mov_b32_e32 v72, v218
	v_mov_b32_e32 v73, v219
	v_mov_b32_e32 v82, v220
	v_mov_b32_e32 v83, v221
	v_mov_b32_e32 v84, v222
	v_mov_b32_e32 v85, v223
	v_mov_b32_e32 v86, v216
	v_mov_b32_e32 v87, v217
	v_mov_b32_e32 v88, v218
	v_mov_b32_e32 v89, v219
	v_mov_b32_e32 v34, v212
	v_mov_b32_e32 v35, v213
	v_mov_b32_e32 v36, v214
	v_mov_b32_e32 v37, v215
	v_mov_b32_e32 v38, v208
	v_mov_b32_e32 v39, v209
	v_mov_b32_e32 v40, v210
	v_mov_b32_e32 v41, v211
	v_mov_b32_e32 v50, v212
	v_mov_b32_e32 v51, v213
	v_mov_b32_e32 v52, v214
	v_mov_b32_e32 v53, v215
	v_mov_b32_e32 v58, v208
	v_mov_b32_e32 v59, v209
	v_mov_b32_e32 v60, v210
	v_mov_b32_e32 v61, v211
	v_mov_b32_e32 v74, v212
	v_mov_b32_e32 v75, v213
	v_mov_b32_e32 v76, v214
	v_mov_b32_e32 v77, v215
	v_mov_b32_e32 v78, v208
	v_mov_b32_e32 v79, v209
	v_mov_b32_e32 v80, v210
	v_mov_b32_e32 v81, v211
	v_mov_b32_e32 v90, v212
	v_mov_b32_e32 v91, v213
	v_mov_b32_e32 v92, v214
	v_mov_b32_e32 v93, v215
	v_mov_b32_e32 v94, v208
	v_mov_b32_e32 v95, v209
	v_mov_b32_e32 v96, v210
	v_mov_b32_e32 v97, v211
	v_mov_b32_e32 v98, v220
	v_mov_b32_e32 v99, v221
	v_mov_b32_e32 v100, v222
	v_mov_b32_e32 v101, v223
	v_mov_b32_e32 v102, v216
	v_mov_b32_e32 v103, v217
	v_mov_b32_e32 v104, v218
	v_mov_b32_e32 v105, v219
	v_mov_b32_e32 v114, v220
	v_mov_b32_e32 v115, v221
	v_mov_b32_e32 v116, v222
	v_mov_b32_e32 v117, v223
	v_mov_b32_e32 v118, v216
	v_mov_b32_e32 v119, v217
	v_mov_b32_e32 v120, v218
	v_mov_b32_e32 v121, v219
	v_mov_b32_e32 v130, v220
	v_mov_b32_e32 v131, v221
	v_mov_b32_e32 v132, v222
	v_mov_b32_e32 v133, v223
	v_mov_b32_e32 v134, v216
	v_mov_b32_e32 v135, v217
	v_mov_b32_e32 v136, v218
	v_mov_b32_e32 v137, v219
	v_mov_b32_e32 v146, v220
	v_mov_b32_e32 v147, v221
	v_mov_b32_e32 v148, v222
	v_mov_b32_e32 v149, v223
	v_mov_b32_e32 v150, v216
	v_mov_b32_e32 v151, v217
	v_mov_b32_e32 v152, v218
	v_mov_b32_e32 v153, v219
	v_mov_b32_e32 v106, v212
	v_mov_b32_e32 v107, v213
	v_mov_b32_e32 v108, v214
	v_mov_b32_e32 v109, v215
	v_mov_b32_e32 v110, v208
	v_mov_b32_e32 v111, v209
	v_mov_b32_e32 v112, v210
	v_mov_b32_e32 v113, v211
	v_mov_b32_e32 v122, v212
	v_mov_b32_e32 v123, v213
	v_mov_b32_e32 v124, v214
	v_mov_b32_e32 v125, v215
	v_mov_b32_e32 v126, v208
	v_mov_b32_e32 v127, v209
	v_mov_b32_e32 v128, v210
	v_mov_b32_e32 v129, v211
	v_mov_b32_e32 v138, v212
	v_mov_b32_e32 v139, v213
	v_mov_b32_e32 v140, v214
	v_mov_b32_e32 v141, v215
	v_mov_b32_e32 v142, v208
	v_mov_b32_e32 v143, v209
	v_mov_b32_e32 v144, v210
	v_mov_b32_e32 v145, v211
	v_mov_b32_e32 v154, v212
	v_mov_b32_e32 v155, v213
	v_mov_b32_e32 v156, v214
	v_mov_b32_e32 v157, v215
	v_mov_b32_e32 v158, v208
	v_mov_b32_e32 v159, v209
	v_mov_b32_e32 v160, v210
	v_mov_b32_e32 v161, v211
	v_mov_b32_e32 v62, v216
	v_mov_b32_e32 v63, v217
	v_mov_b32_e32 v64, v218
	v_mov_b32_e32 v65, v219
	v_mov_b32_e32 v54, v220
	v_mov_b32_e32 v55, v221
	v_mov_b32_e32 v56, v222
	v_mov_b32_e32 v57, v223
	v_mov_b32_e32 v46, v216
	v_mov_b32_e32 v47, v217
	v_mov_b32_e32 v48, v218
	v_mov_b32_e32 v49, v219
	v_mov_b32_e32 v42, v220
	v_mov_b32_e32 v43, v221
	v_mov_b32_e32 v44, v222
	v_mov_b32_e32 v45, v223

; #define LAS __attribute__((address_space(3)))
; __device__ __forceinline__ unsigned pk4_fp8(float a, float b, float c, float d) { int w = 0; w = __builtin_amdgcn_cvt_pk_fp8_f32(a, b, w, false); w = __builtin_amdgcn_cvt_pk_fp8_f32(c, d, w, true); return (unsigned)w; }
; __device__ __forceinline__ float swiglu1(float g, float l) {
;     g = fminf(g, 7.0f); l = fminf(fmaxf(l, -7.0f), 7.0f);
;     const float s = __builtin_amdgcn_rcpf(1.0f + __expf(-1.702f * g));
;     return g * s * (l + 1.0f);
; }
;     __device__ __forceinline__ void operator()(const f32x4 (&acc)[2][2][4][2], const Unit& u, int wr, int wc, int fr, int fq) const {
;     ...
;         for (int ai = 0; ai < 2; ++ai) {
; #pragma unroll
;             for (int m = 0; m < 4; ++m)
; #pragma unroll
;                 for (int bj = 0; bj < 2; ++bj) { const f32x4 v0 = acc[ai][bj][m][0] * scale + bv[bj][0], v1 = acc[ai][bj][m][1] * scale + bv[bj][1];
;                     *(LAS unsigned*)(wp + m * (32 * STG8_PITCH) + 64 * bj) = pk4_fp8(swiglu1(v0[0], v0[1]), swiglu1(v0[2], v0[3]), swiglu1(v1[0], v1[1]), swiglu1(v1[2], v1[3])); }
.LBB0_1010:
	s_cmp_eq_u32 s42, s46
	s_cselect_b32 s55, s23, s19
	s_ashr_i32 s2, s23, 31
	s_lshr_b32 s2, s2, 28
	s_add_i32 s3, s23, s2
	s_and_b32 s3, s3, -16
	s_sub_i32 s23, s23, s3
	s_ashr_i32 s2, s55, 31
	s_lshr_b32 s2, s2, 28
	s_add_i32 s3, s55, s2
	s_ashr_i32 s2, s3, 4
	s_and_b32 s3, s3, -16
	s_sub_i32 s54, s55, s3
	s_ashr_i32 s3, s2, 31
	s_lshl_b64 s[2:3], s[2:3], 14
	v_readlane_b32 s52, v254, 0
	v_lshl_or_b32 v2, s54, 8, v200
	v_readlane_b32 s53, v254, 1
	s_add_u32 s2, s52, s2
	s_addc_u32 s3, s53, s3
	v_ashrrev_i32_e32 v3, 31, v2
	s_nop 15
	s_nop 15
	v_lshl_add_u64 v[2:3], v[2:3], 2, s[2:3]
	global_load_dwordx4 v[208:211], v[2:3], off
	global_load_dwordx4 v[212:215], v[2:3], off offset:16
	global_load_dwordx4 v[216:219], v[2:3], off offset:512
	global_load_dwordx4 v[220:223], v[2:3], off offset:528
	v_lshl_or_b32 v18, s22, 8, v201
	v_ashrrev_i32_e32 v19, 31, v18
	v_lshlrev_b64 v[18:19], 11, v[18:19]
	s_lshl_b32 s22, s23, 7
	v_lshl_add_u64 v[18:19], s[8:9], 0, v[18:19]
	s_ashr_i32 s23, s22, 31
	v_lshl_add_u64 v[18:19], v[18:19], 0, s[22:23]
	v_lshl_add_u64 v[18:19], v[18:19], 0, v[170:171]
	s_cmp_eq_u32 s42, s46
	s_mov_b64 s[2:3], -1
	v_readlane_b32 s54, v254, 2
	v_readlane_b32 s55, v254, 3
	v_readlane_b32 s56, v254, 4
	v_readlane_b32 s57, v254, 5
	v_readlane_b32 s58, v254, 6
	v_readlane_b32 s59, v254, 7
	v_add_u32_e32 v22, 0x1000, v202
	v_add_u32_e32 v23, 0x2400, v202
	v_add_u32_e32 v24, 0x3400, v202
	v_min_f32_e32 v158, 0x43e00000, v158
	v_min_f32_e32 v160, 0x43e00000, v160
	v_min_f32_e32 v154, 0x43e00000, v154
	v_min_f32_e32 v156, 0x43e00000, v156
	v_mul_f32_e32 v2, 0xbd1d265f, v158
	v_mul_f32_e32 v3, 0xbd1d265f, v160
	v_mul_f32_e32 v4, 0xbd1d265f, v154
	v_mul_f32_e32 v5, 0xbd1d265f, v156
	v_exp_f32_e32 v2, v2
	v_exp_f32_e32 v3, v3
	v_exp_f32_e32 v4, v4
	v_exp_f32_e32 v5, v5
	v_fma_f32 v2, v2, v246, v246
	v_fma_f32 v3, v3, v246, v246
	v_fma_f32 v4, v4, v246, v246
	v_fma_f32 v5, v5, v246, v246
	v_rcp_f32_e32 v2, v2
	v_rcp_f32_e32 v3, v3
	v_rcp_f32_e32 v4, v4
	v_rcp_f32_e32 v5, v5
	v_med3_f32 v159, v159, s47, v204
	v_med3_f32 v161, v161, s47, v204
	v_med3_f32 v155, v155, s47, v204
	v_med3_f32 v157, v157, s47, v204
	v_mul_f32_e32 v158, v158, v2
	v_mul_f32_e32 v160, v160, v3
	v_mul_f32_e32 v154, v154, v4
	v_mul_f32_e32 v156, v156, v5
	v_mul_f32_e32 v158, v158, v159
	v_mul_f32_e32 v160, v160, v161
	v_mul_f32_e32 v154, v154, v155
	v_mul_f32_e32 v156, v156, v157
	v_cvt_pk_fp8_f32 v6, v158, v160
	v_cvt_pk_fp8_f32 v6, v154, v156 op_sel:[0,0,1]
	v_min_f32_e32 v150, 0x43e00000, v150
	v_min_f32_e32 v152, 0x43e00000, v152
	v_min_f32_e32 v146, 0x43e00000, v146
	v_min_f32_e32 v148, 0x43e00000, v148
	v_mul_f32_e32 v2, 0xbd1d265f, v150
	v_mul_f32_e32 v3, 0xbd1d265f, v152
	v_mul_f32_e32 v4, 0xbd1d265f, v146
	v_mul_f32_e32 v5, 0xbd1d265f, v148
	v_exp_f32_e32 v2, v2
	v_exp_f32_e32 v3, v3
	v_exp_f32_e32 v4, v4
	v_exp_f32_e32 v5, v5
	v_fma_f32 v2, v2, v246, v246
	v_fma_f32 v3, v3, v246, v246
	v_fma_f32 v4, v4, v246, v246
	v_fma_f32 v5, v5, v246, v246
	v_rcp_f32_e32 v2, v2
	v_rcp_f32_e32 v3, v3
	v_rcp_f32_e32 v4, v4
	v_rcp_f32_e32 v5, v5
	v_med3_f32 v151, v151, s47, v204
	v_med3_f32 v153, v153, s47, v204
	v_med3_f32 v147, v147, s47, v204
	v_med3_f32 v149, v149, s47, v204
	v_mul_f32_e32 v150, v150, v2
	v_mul_f32_e32 v152, v152, v3
	v_mul_f32_e32 v146, v146, v4
	v_mul_f32_e32 v148, v148, v5
	v_mul_f32_e32 v150, v150, v151
	v_mul_f32_e32 v152, v152, v153
	v_mul_f32_e32 v146, v146, v147
	v_mul_f32_e32 v148, v148, v149
	v_cvt_pk_fp8_f32 v7, v150, v152
	v_cvt_pk_fp8_f32 v7, v146, v148 op_sel:[0,0,1]
	v_min_f32_e32 v142, 0x43e00000, v142
	v_min_f32_e32 v144, 0x43e00000, v144
	v_min_f32_e32 v138, 0x43e00000, v138
	v_min_f32_e32 v140, 0x43e00000, v140
	v_mul_f32_e32 v2, 0xbd1d265f, v142
	v_mul_f32_e32 v3, 0xbd1d265f, v144
	v_mul_f32_e32 v4, 0xbd1d265f, v138
	v_mul_f32_e32 v5, 0xbd1d265f, v140
	v_exp_f32_e32 v2, v2
	v_exp_f32_e32 v3, v3
	v_exp_f32_e32 v4, v4
	v_exp_f32_e32 v5, v5
	v_fma_f32 v2, v2, v246, v246
	v_fma_f32 v3, v3, v246, v246
	v_fma_f32 v4, v4, v246, v246
	v_fma_f32 v5, v5, v246, v246
	v_rcp_f32_e32 v2, v2
	v_rcp_f32_e32 v3, v3
	v_rcp_f32_e32 v4, v4
	v_rcp_f32_e32 v5, v5
	v_med3_f32 v143, v143, s47, v204
	v_med3_f32 v145, v145, s47, v204
	v_med3_f32 v139, v139, s47, v204
	v_med3_f32 v141, v141, s47, v204
	v_mul_f32_e32 v142, v142, v2
	v_mul_f32_e32 v144, v144, v3
	v_mul_f32_e32 v138, v138, v4
	v_mul_f32_e32 v140, v140, v5
	v_mul_f32_e32 v142, v142, v143
	v_mul_f32_e32 v144, v144, v145
	v_mul_f32_e32 v138, v138, v139
	v_mul_f32_e32 v140, v140, v141
	v_cvt_pk_fp8_f32 v8, v142, v144
	v_cvt_pk_fp8_f32 v8, v138, v140 op_sel:[0,0,1]
	v_min_f32_e32 v134, 0x43e00000, v134
	v_min_f32_e32 v136, 0x43e00000, v136
	v_min_f32_e32 v130, 0x43e00000, v130
	v_min_f32_e32 v132, 0x43e00000, v132
	v_mul_f32_e32 v2, 0xbd1d265f, v134
	v_mul_f32_e32 v3, 0xbd1d265f, v136
	v_mul_f32_e32 v4, 0xbd1d265f, v130
	v_mul_f32_e32 v5, 0xbd1d265f, v132
	v_exp_f32_e32 v2, v2
	v_exp_f32_e32 v3, v3
	v_exp_f32_e32 v4, v4
	v_exp_f32_e32 v5, v5
	v_fma_f32 v2, v2, v246, v246
	v_fma_f32 v3, v3, v246, v246
	v_fma_f32 v4, v4, v246, v246
	v_fma_f32 v5, v5, v246, v246
	v_rcp_f32_e32 v2, v2
	v_rcp_f32_e32 v3, v3
	v_rcp_f32_e32 v4, v4
	v_rcp_f32_e32 v5, v5
	v_med3_f32 v135, v135, s47, v204
	v_med3_f32 v137, v137, s47, v204
	v_med3_f32 v131, v131, s47, v204
	v_med3_f32 v133, v133, s47, v204
	v_mul_f32_e32 v134, v134, v2
	v_mul_f32_e32 v136, v136, v3
	v_mul_f32_e32 v130, v130, v4
	v_mul_f32_e32 v132, v132, v5
	v_mul_f32_e32 v134, v134, v135
	v_mul_f32_e32 v136, v136, v137
	v_mul_f32_e32 v130, v130, v131
	v_mul_f32_e32 v132, v132, v133
	v_cvt_pk_fp8_f32 v9, v134, v136
	v_cvt_pk_fp8_f32 v9, v130, v132 op_sel:[0,0,1]
; #define LAS __attribute__((address_space(3)))
; __device__ __forceinline__ unsigned pk4_fp8(float a, float b, float c, float d) { int w = 0; w = __builtin_amdgcn_cvt_pk_fp8_f32(a, b, w, false); w = __builtin_amdgcn_cvt_pk_fp8_f32(c, d, w, true); return (unsigned)w; }
;     __device__ __forceinline__ void operator()(const f32x4 (&acc)[2][2][4][2], const Unit& u, int wr, int wc, int fr, int fq) const {
;     ...
;                 for (int bj = 0; bj < 2; ++bj) { const f32x4 v0 = acc[ai][bj][m][0] * scale + bv[bj][0], v1 = acc[ai][bj][m][1] * scale + bv[bj][1];
;                     *(LAS unsigned*)(wp + m * (32 * STG8_PITCH) + 64 * bj) = pk4_fp8(swiglu1(v0[0], v0[1]), swiglu1(v0[2], v0[3]), swiglu1(v1[0], v1[1]), swiglu1(v1[2], v1[3])); }
;             asm volatile("s_waitcnt lgkmcnt(0)" ::: "memory"); __builtin_amdgcn_s_barrier(); asm volatile("" ::: "memory");
; #pragma unroll
;             for (int k2 = 0; k2 < 2; ++k2) { const int m = ms + 2 * k2;
;                 *(u32x4*)(gp + (size_t)(ai * HALF + m * 16) * ldc) = *(const LAS u32x4*)(rp + m * (32 * STG8_PITCH)); }
	v_min_f32_e32 v126, 0x43e00000, v126
	v_min_f32_e32 v128, 0x43e00000, v128
	v_min_f32_e32 v122, 0x43e00000, v122
	v_min_f32_e32 v124, 0x43e00000, v124
	v_mul_f32_e32 v2, 0xbd1d265f, v126
	v_mul_f32_e32 v3, 0xbd1d265f, v128
	v_mul_f32_e32 v4, 0xbd1d265f, v122
	v_mul_f32_e32 v5, 0xbd1d265f, v124
	v_exp_f32_e32 v2, v2
	v_exp_f32_e32 v3, v3
	v_exp_f32_e32 v4, v4
	v_exp_f32_e32 v5, v5
	v_fma_f32 v2, v2, v246, v246
	v_fma_f32 v3, v3, v246, v246
	v_fma_f32 v4, v4, v246, v246
	v_fma_f32 v5, v5, v246, v246
	v_rcp_f32_e32 v2, v2
	v_rcp_f32_e32 v3, v3
	v_rcp_f32_e32 v4, v4
	v_rcp_f32_e32 v5, v5
	v_med3_f32 v127, v127, s47, v204
	v_med3_f32 v129, v129, s47, v204
	v_med3_f32 v123, v123, s47, v204
	v_med3_f32 v125, v125, s47, v204
	v_mul_f32_e32 v126, v126, v2
	v_mul_f32_e32 v128, v128, v3
	v_mul_f32_e32 v122, v122, v4
	v_mul_f32_e32 v124, v124, v5
	v_mul_f32_e32 v126, v126, v127
	v_mul_f32_e32 v128, v128, v129
	v_mul_f32_e32 v122, v122, v123
	v_mul_f32_e32 v124, v124, v125
	v_cvt_pk_fp8_f32 v10, v126, v128
	v_cvt_pk_fp8_f32 v10, v122, v124 op_sel:[0,0,1]
	v_min_f32_e32 v118, 0x43e00000, v118
	v_min_f32_e32 v120, 0x43e00000, v120
	v_min_f32_e32 v114, 0x43e00000, v114
	v_min_f32_e32 v116, 0x43e00000, v116
	v_mul_f32_e32 v2, 0xbd1d265f, v118
	v_mul_f32_e32 v3, 0xbd1d265f, v120
	v_mul_f32_e32 v4, 0xbd1d265f, v114
	v_mul_f32_e32 v5, 0xbd1d265f, v116
	v_exp_f32_e32 v2, v2
	v_exp_f32_e32 v3, v3
	v_exp_f32_e32 v4, v4
	v_exp_f32_e32 v5, v5
	v_fma_f32 v2, v2, v246, v246
	v_fma_f32 v3, v3, v246, v246
	v_fma_f32 v4, v4, v246, v246
	v_fma_f32 v5, v5, v246, v246
	v_rcp_f32_e32 v2, v2
	v_rcp_f32_e32 v3, v3
	v_rcp_f32_e32 v4, v4
	v_rcp_f32_e32 v5, v5
	v_med3_f32 v119, v119, s47, v204
	v_med3_f32 v121, v121, s47, v204
	v_med3_f32 v115, v115, s47, v204
	v_med3_f32 v117, v117, s47, v204
	v_mul_f32_e32 v118, v118, v2
	v_mul_f32_e32 v120, v120, v3
	v_mul_f32_e32 v114, v114, v4
	v_mul_f32_e32 v116, v116, v5
	v_mul_f32_e32 v118, v118, v119
	v_mul_f32_e32 v120, v120, v121
	v_mul_f32_e32 v114, v114, v115
	v_mul_f32_e32 v116, v116, v117
	v_cvt_pk_fp8_f32 v11, v118, v120
	v_cvt_pk_fp8_f32 v11, v114, v116 op_sel:[0,0,1]
	v_min_f32_e32 v110, 0x43e00000, v110
	v_min_f32_e32 v112, 0x43e00000, v112
	v_min_f32_e32 v106, 0x43e00000, v106
	v_min_f32_e32 v108, 0x43e00000, v108
	v_mul_f32_e32 v2, 0xbd1d265f, v110
	v_mul_f32_e32 v3, 0xbd1d265f, v112
	v_mul_f32_e32 v4, 0xbd1d265f, v106
	v_mul_f32_e32 v5, 0xbd1d265f, v108
	v_exp_f32_e32 v2, v2
	v_exp_f32_e32 v3, v3
	v_exp_f32_e32 v4, v4
	v_exp_f32_e32 v5, v5
	v_fma_f32 v2, v2, v246, v246
	v_fma_f32 v3, v3, v246, v246
	v_fma_f32 v4, v4, v246, v246
	v_fma_f32 v5, v5, v246, v246
	v_rcp_f32_e32 v2, v2
	v_rcp_f32_e32 v3, v3
	v_rcp_f32_e32 v4, v4
	v_rcp_f32_e32 v5, v5
	v_med3_f32 v111, v111, s47, v204
	v_med3_f32 v113, v113, s47, v204
	v_med3_f32 v107, v107, s47, v204
	v_med3_f32 v109, v109, s47, v204
	v_mul_f32_e32 v110, v110, v2
	v_mul_f32_e32 v112, v112, v3
	v_mul_f32_e32 v106, v106, v4
	v_mul_f32_e32 v108, v108, v5
	v_mul_f32_e32 v110, v110, v111
	v_mul_f32_e32 v112, v112, v113
	v_mul_f32_e32 v106, v106, v107
	v_mul_f32_e32 v108, v108, v109
	v_cvt_pk_fp8_f32 v12, v110, v112
	v_cvt_pk_fp8_f32 v12, v106, v108 op_sel:[0,0,1]
	v_min_f32_e32 v102, 0x43e00000, v102
	v_min_f32_e32 v104, 0x43e00000, v104
	v_min_f32_e32 v98, 0x43e00000, v98
	v_min_f32_e32 v100, 0x43e00000, v100
	v_mul_f32_e32 v2, 0xbd1d265f, v102
	v_mul_f32_e32 v3, 0xbd1d265f, v104
	v_mul_f32_e32 v4, 0xbd1d265f, v98
	v_mul_f32_e32 v5, 0xbd1d265f, v100
	v_exp_f32_e32 v2, v2
	v_exp_f32_e32 v3, v3
	v_exp_f32_e32 v4, v4
	v_exp_f32_e32 v5, v5
	v_fma_f32 v2, v2, v246, v246
	v_fma_f32 v3, v3, v246, v246
	v_fma_f32 v4, v4, v246, v246
	v_fma_f32 v5, v5, v246, v246
	v_rcp_f32_e32 v2, v2
	v_rcp_f32_e32 v3, v3
	v_rcp_f32_e32 v4, v4
	v_rcp_f32_e32 v5, v5
	v_med3_f32 v103, v103, s47, v204
	v_med3_f32 v105, v105, s47, v204
	v_med3_f32 v99, v99, s47, v204
	v_med3_f32 v101, v101, s47, v204
	v_mul_f32_e32 v102, v102, v2
	v_mul_f32_e32 v104, v104, v3
	v_mul_f32_e32 v98, v98, v4
	v_mul_f32_e32 v100, v100, v5
	v_mul_f32_e32 v102, v102, v103
	v_mul_f32_e32 v104, v104, v105
	v_mul_f32_e32 v98, v98, v99
	v_mul_f32_e32 v100, v100, v101
	v_cvt_pk_fp8_f32 v13, v102, v104
	v_cvt_pk_fp8_f32 v13, v98, v100 op_sel:[0,0,1]
	ds_write2_b32 v202, v6, v7 offset1:16
	ds_write2_b32 v22, v8, v9 offset0:128 offset1:144
	ds_write2_b32 v23, v10, v11 offset1:16
	ds_write2_b32 v24, v12, v13 offset0:128 offset1:144
	s_waitcnt lgkmcnt(0)
	s_barrier
	ds_read_b128 v[26:29], v203
	ds_read_b128 v[30:33], v203 offset:9216
	v_lshl_add_u64 v[20:21], v[18:19], 0, v[172:173]
	v_lshl_add_u64 v[18:19], v[18:19], 0, v[174:175]
	s_waitcnt lgkmcnt(1)
	global_store_dwordx4 v[20:21], v[26:29], off
	s_waitcnt lgkmcnt(0)
	global_store_dwordx4 v[18:19], v[30:33], off
	s_waitcnt lgkmcnt(0)
	s_barrier
; #define LAS __attribute__((address_space(3)))
; __device__ __forceinline__ unsigned pk4_fp8(float a, float b, float c, float d) { int w = 0; w = __builtin_amdgcn_cvt_pk_fp8_f32(a, b, w, false); w = __builtin_amdgcn_cvt_pk_fp8_f32(c, d, w, true); return (unsigned)w; }
; __device__ __forceinline__ float swiglu1(float g, float l) {
;     g = fminf(g, 7.0f); l = fminf(fmaxf(l, -7.0f), 7.0f);
;     const float s = __builtin_amdgcn_rcpf(1.0f + __expf(-1.702f * g));
;     return g * s * (l + 1.0f);
; }
;     __device__ __forceinline__ void operator()(const f32x4 (&acc)[2][2][4][2], const Unit& u, int wr, int wc, int fr, int fq) const {
;     ...
;                 for (int bj = 0; bj < 2; ++bj) { const f32x4 v0 = acc[ai][bj][m][0] * scale + bv[bj][0], v1 = acc[ai][bj][m][1] * scale + bv[bj][1];
;                     *(LAS unsigned*)(wp + m * (32 * STG8_PITCH) + 64 * bj) = pk4_fp8(swiglu1(v0[0], v0[1]), swiglu1(v0[2], v0[3]), swiglu1(v1[0], v1[1]), swiglu1(v1[2], v1[3])); }
	v_min_f32_e32 v94, 0x43e00000, v94
	v_min_f32_e32 v96, 0x43e00000, v96
	v_min_f32_e32 v90, 0x43e00000, v90
	v_min_f32_e32 v92, 0x43e00000, v92
	v_mul_f32_e32 v2, 0xbd1d265f, v94
	v_mul_f32_e32 v3, 0xbd1d265f, v96
	v_mul_f32_e32 v4, 0xbd1d265f, v90
	v_mul_f32_e32 v5, 0xbd1d265f, v92
	v_exp_f32_e32 v2, v2
	v_exp_f32_e32 v3, v3
	v_exp_f32_e32 v4, v4
	v_exp_f32_e32 v5, v5
	v_fma_f32 v2, v2, v246, v246
	v_fma_f32 v3, v3, v246, v246
	v_fma_f32 v4, v4, v246, v246
	v_fma_f32 v5, v5, v246, v246
	v_rcp_f32_e32 v2, v2
	v_rcp_f32_e32 v3, v3
	v_rcp_f32_e32 v4, v4
	v_rcp_f32_e32 v5, v5
	v_med3_f32 v95, v95, s47, v204
	v_med3_f32 v97, v97, s47, v204
	v_med3_f32 v91, v91, s47, v204
	v_med3_f32 v93, v93, s47, v204
	v_mul_f32_e32 v94, v94, v2
	v_mul_f32_e32 v96, v96, v3
	v_mul_f32_e32 v90, v90, v4
	v_mul_f32_e32 v92, v92, v5
	v_mul_f32_e32 v94, v94, v95
	v_mul_f32_e32 v96, v96, v97
	v_mul_f32_e32 v90, v90, v91
	v_mul_f32_e32 v92, v92, v93
	v_cvt_pk_fp8_f32 v6, v94, v96
	v_cvt_pk_fp8_f32 v6, v90, v92 op_sel:[0,0,1]
	v_min_f32_e32 v86, 0x43e00000, v86
	v_min_f32_e32 v88, 0x43e00000, v88
	v_min_f32_e32 v82, 0x43e00000, v82
	v_min_f32_e32 v84, 0x43e00000, v84
	v_mul_f32_e32 v2, 0xbd1d265f, v86
	v_mul_f32_e32 v3, 0xbd1d265f, v88
	v_mul_f32_e32 v4, 0xbd1d265f, v82
	v_mul_f32_e32 v5, 0xbd1d265f, v84
	v_exp_f32_e32 v2, v2
	v_exp_f32_e32 v3, v3
	v_exp_f32_e32 v4, v4
	v_exp_f32_e32 v5, v5
	v_fma_f32 v2, v2, v246, v246
	v_fma_f32 v3, v3, v246, v246
	v_fma_f32 v4, v4, v246, v246
	v_fma_f32 v5, v5, v246, v246
	v_rcp_f32_e32 v2, v2
	v_rcp_f32_e32 v3, v3
	v_rcp_f32_e32 v4, v4
	v_rcp_f32_e32 v5, v5
	v_med3_f32 v87, v87, s47, v204
	v_med3_f32 v89, v89, s47, v204
	v_med3_f32 v83, v83, s47, v204
	v_med3_f32 v85, v85, s47, v204
	v_mul_f32_e32 v86, v86, v2
	v_mul_f32_e32 v88, v88, v3
	v_mul_f32_e32 v82, v82, v4
	v_mul_f32_e32 v84, v84, v5
	v_mul_f32_e32 v86, v86, v87
	v_mul_f32_e32 v88, v88, v89
	v_mul_f32_e32 v82, v82, v83
	v_mul_f32_e32 v84, v84, v85
	v_cvt_pk_fp8_f32 v7, v86, v88
	v_cvt_pk_fp8_f32 v7, v82, v84 op_sel:[0,0,1]
	v_min_f32_e32 v78, 0x43e00000, v78
	v_min_f32_e32 v80, 0x43e00000, v80
	v_min_f32_e32 v74, 0x43e00000, v74
	v_min_f32_e32 v76, 0x43e00000, v76
	v_mul_f32_e32 v2, 0xbd1d265f, v78
	v_mul_f32_e32 v3, 0xbd1d265f, v80
	v_mul_f32_e32 v4, 0xbd1d265f, v74
	v_mul_f32_e32 v5, 0xbd1d265f, v76
	v_exp_f32_e32 v2, v2
	v_exp_f32_e32 v3, v3
	v_exp_f32_e32 v4, v4
	v_exp_f32_e32 v5, v5
	v_fma_f32 v2, v2, v246, v246
	v_fma_f32 v3, v3, v246, v246
	v_fma_f32 v4, v4, v246, v246
	v_fma_f32 v5, v5, v246, v246
	v_rcp_f32_e32 v2, v2
	v_rcp_f32_e32 v3, v3
	v_rcp_f32_e32 v4, v4
	v_rcp_f32_e32 v5, v5
	v_med3_f32 v79, v79, s47, v204
	v_med3_f32 v81, v81, s47, v204
	v_med3_f32 v75, v75, s47, v204
	v_med3_f32 v77, v77, s47, v204
	v_mul_f32_e32 v78, v78, v2
	v_mul_f32_e32 v80, v80, v3
	v_mul_f32_e32 v74, v74, v4
	v_mul_f32_e32 v76, v76, v5
	v_mul_f32_e32 v78, v78, v79
	v_mul_f32_e32 v80, v80, v81
	v_mul_f32_e32 v74, v74, v75
	v_mul_f32_e32 v76, v76, v77
	v_cvt_pk_fp8_f32 v8, v78, v80
	v_cvt_pk_fp8_f32 v8, v74, v76 op_sel:[0,0,1]
	v_min_f32_e32 v70, 0x43e00000, v70
	v_min_f32_e32 v72, 0x43e00000, v72
	v_min_f32_e32 v66, 0x43e00000, v66
	v_min_f32_e32 v68, 0x43e00000, v68
	v_mul_f32_e32 v2, 0xbd1d265f, v70
	v_mul_f32_e32 v3, 0xbd1d265f, v72
	v_mul_f32_e32 v4, 0xbd1d265f, v66
	v_mul_f32_e32 v5, 0xbd1d265f, v68
	v_exp_f32_e32 v2, v2
	v_exp_f32_e32 v3, v3
	v_exp_f32_e32 v4, v4
	v_exp_f32_e32 v5, v5
	v_fma_f32 v2, v2, v246, v246
	v_fma_f32 v3, v3, v246, v246
	v_fma_f32 v4, v4, v246, v246
	v_fma_f32 v5, v5, v246, v246
	v_rcp_f32_e32 v2, v2
	v_rcp_f32_e32 v3, v3
	v_rcp_f32_e32 v4, v4
	v_rcp_f32_e32 v5, v5
	v_med3_f32 v71, v71, s47, v204
	v_med3_f32 v73, v73, s47, v204
	v_med3_f32 v67, v67, s47, v204
	v_med3_f32 v69, v69, s47, v204
	v_mul_f32_e32 v70, v70, v2
	v_mul_f32_e32 v72, v72, v3
	v_mul_f32_e32 v66, v66, v4
	v_mul_f32_e32 v68, v68, v5
	v_mul_f32_e32 v70, v70, v71
	v_mul_f32_e32 v72, v72, v73
	v_mul_f32_e32 v66, v66, v67
	v_mul_f32_e32 v68, v68, v69
	v_cvt_pk_fp8_f32 v9, v70, v72
	v_cvt_pk_fp8_f32 v9, v66, v68 op_sel:[0,0,1]
	v_min_f32_e32 v58, 0x43e00000, v58
	v_min_f32_e32 v60, 0x43e00000, v60
	v_min_f32_e32 v50, 0x43e00000, v50
	v_min_f32_e32 v52, 0x43e00000, v52
	v_mul_f32_e32 v2, 0xbd1d265f, v58
	v_mul_f32_e32 v3, 0xbd1d265f, v60
	v_mul_f32_e32 v4, 0xbd1d265f, v50
	v_mul_f32_e32 v5, 0xbd1d265f, v52
	v_exp_f32_e32 v2, v2
	v_exp_f32_e32 v3, v3
	v_exp_f32_e32 v4, v4
	v_exp_f32_e32 v5, v5
	v_fma_f32 v2, v2, v246, v246
	v_fma_f32 v3, v3, v246, v246
	v_fma_f32 v4, v4, v246, v246
	v_fma_f32 v5, v5, v246, v246
	v_rcp_f32_e32 v2, v2
	v_rcp_f32_e32 v3, v3
	v_rcp_f32_e32 v4, v4
	v_rcp_f32_e32 v5, v5
	v_med3_f32 v59, v59, s47, v204
	v_med3_f32 v61, v61, s47, v204
; #define LAS __attribute__((address_space(3)))
; __device__ __forceinline__ unsigned pk4_fp8(float a, float b, float c, float d) { int w = 0; w = __builtin_amdgcn_cvt_pk_fp8_f32(a, b, w, false); w = __builtin_amdgcn_cvt_pk_fp8_f32(c, d, w, true); return (unsigned)w; }
;     __device__ __forceinline__ void operator()(const f32x4 (&acc)[2][2][4][2], const Unit& u, int wr, int wc, int fr, int fq) const {
;     ...
;                 for (int bj = 0; bj < 2; ++bj) { const f32x4 v0 = acc[ai][bj][m][0] * scale + bv[bj][0], v1 = acc[ai][bj][m][1] * scale + bv[bj][1];
;                     *(LAS unsigned*)(wp + m * (32 * STG8_PITCH) + 64 * bj) = pk4_fp8(swiglu1(v0[0], v0[1]), swiglu1(v0[2], v0[3]), swiglu1(v1[0], v1[1]), swiglu1(v1[2], v1[3])); }
;             asm volatile("s_waitcnt lgkmcnt(0)" ::: "memory"); __builtin_amdgcn_s_barrier(); asm volatile("" ::: "memory");
; #pragma unroll
;             for (int k2 = 0; k2 < 2; ++k2) { const int m = ms + 2 * k2;
;                 *(u32x4*)(gp + (size_t)(ai * HALF + m * 16) * ldc) = *(const LAS u32x4*)(rp + m * (32 * STG8_PITCH)); }
;             asm volatile("s_waitcnt lgkmcnt(0)" ::: "memory"); __builtin_amdgcn_s_barrier(); asm volatile("" ::: "memory");
;         }
	v_med3_f32 v51, v51, s47, v204
	v_med3_f32 v53, v53, s47, v204
	v_mul_f32_e32 v58, v58, v2
	v_mul_f32_e32 v60, v60, v3
	v_mul_f32_e32 v50, v50, v4
	v_mul_f32_e32 v52, v52, v5
	v_mul_f32_e32 v58, v58, v59
	v_mul_f32_e32 v60, v60, v61
	v_mul_f32_e32 v50, v50, v51
	v_mul_f32_e32 v52, v52, v53
	v_cvt_pk_fp8_f32 v10, v58, v60
	v_cvt_pk_fp8_f32 v10, v50, v52 op_sel:[0,0,1]
	v_min_f32_e32 v62, 0x43e00000, v62
	v_min_f32_e32 v64, 0x43e00000, v64
	v_min_f32_e32 v54, 0x43e00000, v54
	v_min_f32_e32 v56, 0x43e00000, v56
	v_mul_f32_e32 v2, 0xbd1d265f, v62
	v_mul_f32_e32 v3, 0xbd1d265f, v64
	v_mul_f32_e32 v4, 0xbd1d265f, v54
	v_mul_f32_e32 v5, 0xbd1d265f, v56
	v_exp_f32_e32 v2, v2
	v_exp_f32_e32 v3, v3
	v_exp_f32_e32 v4, v4
	v_exp_f32_e32 v5, v5
	v_fma_f32 v2, v2, v246, v246
	v_fma_f32 v3, v3, v246, v246
	v_fma_f32 v4, v4, v246, v246
	v_fma_f32 v5, v5, v246, v246
	v_rcp_f32_e32 v2, v2
	v_rcp_f32_e32 v3, v3
	v_rcp_f32_e32 v4, v4
	v_rcp_f32_e32 v5, v5
	v_med3_f32 v63, v63, s47, v204
	v_med3_f32 v65, v65, s47, v204
	v_med3_f32 v55, v55, s47, v204
	v_med3_f32 v57, v57, s47, v204
	v_mul_f32_e32 v62, v62, v2
	v_mul_f32_e32 v64, v64, v3
	v_mul_f32_e32 v54, v54, v4
	v_mul_f32_e32 v56, v56, v5
	v_mul_f32_e32 v62, v62, v63
	v_mul_f32_e32 v64, v64, v65
	v_mul_f32_e32 v54, v54, v55
	v_mul_f32_e32 v56, v56, v57
	v_cvt_pk_fp8_f32 v11, v62, v64
	v_cvt_pk_fp8_f32 v11, v54, v56 op_sel:[0,0,1]
	v_min_f32_e32 v38, 0x43e00000, v38
	v_min_f32_e32 v40, 0x43e00000, v40
	v_min_f32_e32 v34, 0x43e00000, v34
	v_min_f32_e32 v36, 0x43e00000, v36
	v_mul_f32_e32 v2, 0xbd1d265f, v38
	v_mul_f32_e32 v3, 0xbd1d265f, v40
	v_mul_f32_e32 v4, 0xbd1d265f, v34
	v_mul_f32_e32 v5, 0xbd1d265f, v36
	v_exp_f32_e32 v2, v2
	v_exp_f32_e32 v3, v3
	v_exp_f32_e32 v4, v4
	v_exp_f32_e32 v5, v5
	v_fma_f32 v2, v2, v246, v246
	v_fma_f32 v3, v3, v246, v246
	v_fma_f32 v4, v4, v246, v246
	v_fma_f32 v5, v5, v246, v246
	v_rcp_f32_e32 v2, v2
	v_rcp_f32_e32 v3, v3
	v_rcp_f32_e32 v4, v4
	v_rcp_f32_e32 v5, v5
	v_med3_f32 v39, v39, s47, v204
	v_med3_f32 v41, v41, s47, v204
	v_med3_f32 v35, v35, s47, v204
	v_med3_f32 v37, v37, s47, v204
	v_mul_f32_e32 v38, v38, v2
	v_mul_f32_e32 v40, v40, v3
	v_mul_f32_e32 v34, v34, v4
	v_mul_f32_e32 v36, v36, v5
	v_mul_f32_e32 v38, v38, v39
	v_mul_f32_e32 v40, v40, v41
	v_mul_f32_e32 v34, v34, v35
	v_mul_f32_e32 v36, v36, v37
	v_cvt_pk_fp8_f32 v12, v38, v40
	v_cvt_pk_fp8_f32 v12, v34, v36 op_sel:[0,0,1]
	v_min_f32_e32 v46, 0x43e00000, v46
	v_min_f32_e32 v48, 0x43e00000, v48
	v_min_f32_e32 v42, 0x43e00000, v42
	v_min_f32_e32 v44, 0x43e00000, v44
	v_mul_f32_e32 v2, 0xbd1d265f, v46
	v_mul_f32_e32 v3, 0xbd1d265f, v48
	v_mul_f32_e32 v4, 0xbd1d265f, v42
	v_mul_f32_e32 v5, 0xbd1d265f, v44
	v_exp_f32_e32 v2, v2
	v_exp_f32_e32 v3, v3
	v_exp_f32_e32 v4, v4
	v_exp_f32_e32 v5, v5
	v_fma_f32 v2, v2, v246, v246
	v_fma_f32 v3, v3, v246, v246
	v_fma_f32 v4, v4, v246, v246
	v_fma_f32 v5, v5, v246, v246
	v_rcp_f32_e32 v2, v2
	v_rcp_f32_e32 v3, v3
	v_rcp_f32_e32 v4, v4
	v_rcp_f32_e32 v5, v5
	v_med3_f32 v47, v47, s47, v204
	v_med3_f32 v49, v49, s47, v204
	v_med3_f32 v43, v43, s47, v204
	v_med3_f32 v45, v45, s47, v204
	v_mul_f32_e32 v46, v46, v2
	v_mul_f32_e32 v48, v48, v3
	v_mul_f32_e32 v42, v42, v4
	v_mul_f32_e32 v44, v44, v5
	v_mul_f32_e32 v46, v46, v47
	v_mul_f32_e32 v48, v48, v49
	v_mul_f32_e32 v42, v42, v43
	v_mul_f32_e32 v44, v44, v45
	v_cvt_pk_fp8_f32 v13, v46, v48
	v_cvt_pk_fp8_f32 v13, v42, v44 op_sel:[0,0,1]
	ds_write2_b32 v202, v6, v7 offset1:16
	ds_write2_b32 v22, v8, v9 offset0:128 offset1:144
	ds_write2_b32 v23, v10, v11 offset1:16
	ds_write2_b32 v24, v12, v13 offset0:128 offset1:144
	s_waitcnt lgkmcnt(0)
	s_barrier
	ds_read_b128 v[2:5], v203
	ds_read_b128 v[6:9], v203 offset:9216
	v_add_co_u32_e32 v10, vcc, s48, v20
	s_nop 1
	v_addc_co_u32_e32 v11, vcc, 0, v21, vcc
	s_waitcnt lgkmcnt(1)
	global_store_dwordx4 v[10:11], v[2:5], off
	s_nop 1
	v_add_co_u32_e32 v2, vcc, 0x40000, v18
	s_nop 1
	v_addc_co_u32_e32 v3, vcc, 0, v19, vcc
	s_waitcnt lgkmcnt(0)
	global_store_dwordx4 v[2:3], v[6:9], off
	s_waitcnt lgkmcnt(0)
	s_barrier
	s_waitcnt vmcnt(4)
	v_mul_f32_e32 v208, v247, v208
	v_fma_f32 v209, v209, v247, v247
	v_mul_f32_e32 v210, v247, v210
	v_fma_f32 v211, v211, v247, v247
	v_mul_f32_e32 v212, v247, v212
	v_fma_f32 v213, v213, v247, v247
	v_mul_f32_e32 v214, v247, v214
	v_fma_f32 v215, v215, v247, v247
	v_mul_f32_e32 v216, v247, v216
	v_fma_f32 v217, v217, v247, v247
	v_mul_f32_e32 v218, v247, v218
	v_fma_f32 v219, v219, v247, v247
	v_mul_f32_e32 v220, v247, v220
	v_fma_f32 v221, v221, v247, v247
	v_mul_f32_e32 v222, v247, v222
	v_fma_f32 v223, v223, v247, v247
	s_cbranch_scc1 .LBB0_993
	s_andn2_b64 vcc, exec, s[6:7]
	s_cbranch_vccnz .LBB0_992
	s_barrier
	s_branch .LBB0_992
